# stack12 + grid-barrier poll loops back off s_sleep 10 between polls
# baseline (speedup 1.0000x reference)
.LBB0_101:
	global_load_dword v16, v17, s[6:7] sc1
	global_load_dword v1, v17, s[8:9] sc1
	global_load_dword v2, v17, s[10:11] sc1
	global_load_dword v3, v17, s[12:13] sc1
	global_load_dword v4, v17, s[14:15] sc1
	global_load_dword v5, v17, s[16:17] sc1
	global_load_dword v6, v17, s[18:19] sc1
	global_load_dword v7, v17, s[20:21] sc1
	global_load_dword v8, v17, s[22:23] sc1
	global_load_dword v9, v17, s[24:25] sc1
	global_load_dword v10, v17, s[26:27] sc1
	global_load_dword v11, v17, s[28:29] sc1
	global_load_dword v12, v17, s[30:31] sc1
	global_load_dword v13, v17, s[34:35] sc1
	global_load_dword v14, v17, s[36:37] sc1
	global_load_dword v15, v17, s[38:39] sc1
	s_mov_b64 s[40:41], -1
	s_mov_b64 s[42:43], -1
	s_waitcnt vmcnt(14)
	v_add_u32_e32 v18, v1, v16
	s_waitcnt vmcnt(13)
	v_add_u32_e32 v18, v18, v2
	s_waitcnt vmcnt(12)
	v_add_u32_e32 v18, v18, v3
	s_waitcnt vmcnt(11)
	v_add_u32_e32 v18, v18, v4
	s_waitcnt vmcnt(10)
	v_add_u32_e32 v18, v18, v5
	s_waitcnt vmcnt(9)
	v_add_u32_e32 v18, v18, v6
	s_waitcnt vmcnt(8)
	v_add_u32_e32 v18, v18, v7
	s_waitcnt vmcnt(7)
	v_add_u32_e32 v18, v18, v8
	s_waitcnt vmcnt(6)
	v_add_u32_e32 v18, v18, v9
	s_waitcnt vmcnt(5)
	v_add_u32_e32 v18, v18, v10
	s_waitcnt vmcnt(4)
	v_add_u32_e32 v18, v18, v11
	s_waitcnt vmcnt(3)
	v_add_u32_e32 v18, v18, v12
	s_waitcnt vmcnt(2)
	v_add_u32_e32 v18, v18, v13
	s_waitcnt vmcnt(1)
	v_add_u32_e32 v18, v18, v14
	s_waitcnt vmcnt(0)
	v_add_u32_e32 v18, v18, v15
	v_cmp_eq_u32_e32 vcc, s33, v18
	s_cbranch_vccnz .LBB0_100
	s_and_b32 s40, s47, 0xff
	s_cmp_eq_u32 s40, 0
	s_mov_b64 s[40:41], -1
	s_mov_b64 s[44:45], -1
	s_sleep 10
	s_cbranch_scc0 .LBB0_105
	global_load_dword v18, v17, s[4:5] sc1
	s_waitcnt vmcnt(0)
	v_cmp_eq_u32_e32 vcc, 0, v18
	s_cbranch_vccnz .LBB0_107
	s_mov_b64 s[44:45], 0

.LBB0_119:
	s_and_b32 s20, s24, 0xff
	s_mov_b64 s[18:19], -1
	s_cmp_lg_u32 s20, 0
	s_mov_b64 s[22:23], -1
	s_sleep 10
	s_cbranch_scc1 .LBB0_122
	global_load_dword v3, v1, s[10:11] sc1
	s_waitcnt vmcnt(0)
	v_cmp_eq_u32_e32 vcc, 0, v3
	s_cbranch_vccnz .LBB0_124
	s_mov_b64 s[22:23], 0
	s_mov_b64 s[20:21], -1

.LBB0_136:
	s_and_b32 s18, s24, 0xff
	s_cmp_lg_u32 s18, 0
	s_mov_b64 s[20:21], -1
	s_sleep 10
	s_cbranch_scc1 .LBB0_139
	global_load_dword v2, v1, s[10:11] sc1
	s_waitcnt vmcnt(0)
	v_cmp_eq_u32_e32 vcc, 0, v2
	s_cbranch_vccnz .LBB0_141
	s_mov_b64 s[20:21], 0
	s_mov_b64 s[18:19], -1

.LBB0_533:
	global_load_dword v16, v17, s[6:7] sc1
	global_load_dword v1, v17, s[8:9] sc1
	global_load_dword v2, v17, s[10:11] sc1
	global_load_dword v3, v17, s[12:13] sc1
	global_load_dword v4, v17, s[14:15] sc1
	global_load_dword v5, v17, s[16:17] sc1
	global_load_dword v6, v17, s[18:19] sc1
	global_load_dword v7, v17, s[20:21] sc1
	global_load_dword v8, v17, s[22:23] sc1
	global_load_dword v9, v17, s[24:25] sc1
	global_load_dword v10, v17, s[26:27] sc1
	global_load_dword v11, v17, s[28:29] sc1
	global_load_dword v12, v17, s[30:31] sc1
	global_load_dword v13, v17, s[34:35] sc1
	global_load_dword v14, v17, s[36:37] sc1
	global_load_dword v15, v17, s[38:39] sc1
	s_mov_b64 s[40:41], -1
	s_mov_b64 s[42:43], -1
	s_waitcnt vmcnt(14)
	v_add_u32_e32 v18, v1, v16
	s_waitcnt vmcnt(13)
	v_add_u32_e32 v18, v18, v2
	s_waitcnt vmcnt(12)
	v_add_u32_e32 v18, v18, v3
	s_waitcnt vmcnt(11)
	v_add_u32_e32 v18, v18, v4
	s_waitcnt vmcnt(10)
	v_add_u32_e32 v18, v18, v5
	s_waitcnt vmcnt(9)
	v_add_u32_e32 v18, v18, v6
	s_waitcnt vmcnt(8)
	v_add_u32_e32 v18, v18, v7
	s_waitcnt vmcnt(7)
	v_add_u32_e32 v18, v18, v8
	s_waitcnt vmcnt(6)
	v_add_u32_e32 v18, v18, v9
	s_waitcnt vmcnt(5)
	v_add_u32_e32 v18, v18, v10
	s_waitcnt vmcnt(4)
	v_add_u32_e32 v18, v18, v11
	s_waitcnt vmcnt(3)
	v_add_u32_e32 v18, v18, v12
	s_waitcnt vmcnt(2)
	v_add_u32_e32 v18, v18, v13
	s_waitcnt vmcnt(1)
	v_add_u32_e32 v18, v18, v14
	s_waitcnt vmcnt(0)
	v_add_u32_e32 v18, v18, v15
	v_cmp_eq_u32_e32 vcc, s33, v18
	s_cbranch_vccnz .LBB0_532
	s_and_b32 s40, s46, 0xff
	s_cmp_eq_u32 s40, 0
	s_mov_b64 s[40:41], -1
	s_mov_b64 s[44:45], -1
	s_sleep 10
	s_cbranch_scc0 .LBB0_537
	global_load_dword v18, v17, s[4:5] sc1
	s_waitcnt vmcnt(0)
	v_cmp_eq_u32_e32 vcc, 0, v18
	s_cbranch_vccnz .LBB0_539
	s_mov_b64 s[44:45], 0

.LBB0_1358:
	global_load_dword v16, v17, s[8:9] sc1
	global_load_dword v1, v17, s[10:11] sc1
	global_load_dword v2, v17, s[12:13] sc1
	global_load_dword v3, v17, s[14:15] sc1
	global_load_dword v4, v17, s[16:17] sc1
	global_load_dword v5, v17, s[18:19] sc1
	global_load_dword v6, v17, s[20:21] sc1
	global_load_dword v7, v17, s[22:23] sc1
	global_load_dword v8, v17, s[24:25] sc1
	global_load_dword v9, v17, s[26:27] sc1
	global_load_dword v10, v17, s[28:29] sc1
	global_load_dword v11, v17, s[30:31] sc1
	global_load_dword v12, v17, s[34:35] sc1
	global_load_dword v13, v17, s[36:37] sc1
	global_load_dword v14, v17, s[38:39] sc1
	global_load_dword v15, v17, s[40:41] sc1
	s_mov_b64 s[42:43], -1
	s_mov_b64 s[44:45], -1
	s_waitcnt vmcnt(14)
	v_add_u32_e32 v18, v1, v16
	s_waitcnt vmcnt(13)
	v_add_u32_e32 v18, v18, v2
	s_waitcnt vmcnt(12)
	v_add_u32_e32 v18, v18, v3
	s_waitcnt vmcnt(11)
	v_add_u32_e32 v18, v18, v4
	s_waitcnt vmcnt(10)
	v_add_u32_e32 v18, v18, v5
	s_waitcnt vmcnt(9)
	v_add_u32_e32 v18, v18, v6
	s_waitcnt vmcnt(8)
	v_add_u32_e32 v18, v18, v7
	s_waitcnt vmcnt(7)
	v_add_u32_e32 v18, v18, v8
	s_waitcnt vmcnt(6)
	v_add_u32_e32 v18, v18, v9
	s_waitcnt vmcnt(5)
	v_add_u32_e32 v18, v18, v10
	s_waitcnt vmcnt(4)
	v_add_u32_e32 v18, v18, v11
	s_waitcnt vmcnt(3)
	v_add_u32_e32 v18, v18, v12
	s_waitcnt vmcnt(2)
	v_add_u32_e32 v18, v18, v13
	s_waitcnt vmcnt(1)
	v_add_u32_e32 v18, v18, v14
	s_waitcnt vmcnt(0)
	v_add_u32_e32 v18, v18, v15
	v_cmp_eq_u32_e32 vcc, s33, v18
	s_cbranch_vccnz .LBB0_1357
	s_and_b32 s42, s48, 0xff
	s_cmp_eq_u32 s42, 0
	s_mov_b64 s[42:43], -1
	s_mov_b64 s[46:47], -1
	s_sleep 10
	s_cbranch_scc0 .LBB0_1362
	global_load_dword v18, v17, s[6:7] sc1
	s_waitcnt vmcnt(0)
	v_cmp_eq_u32_e32 vcc, 0, v18
	s_cbranch_vccnz .LBB0_1364
	s_mov_b64 s[46:47], 0

.LBB0_1376:
	s_and_b32 s22, s26, 0xff
	s_mov_b64 s[20:21], -1
	s_cmp_lg_u32 s22, 0
	s_mov_b64 s[24:25], -1
	s_sleep 10
	s_cbranch_scc1 .LBB0_1379
	global_load_dword v3, v1, s[12:13] sc1
	s_waitcnt vmcnt(0)
	v_cmp_eq_u32_e32 vcc, 0, v3
	s_cbranch_vccnz .LBB0_1381
	s_mov_b64 s[24:25], 0
	s_mov_b64 s[22:23], -1

.LBB0_1393:
	s_and_b32 s20, s26, 0xff
	s_cmp_lg_u32 s20, 0
	s_mov_b64 s[22:23], -1
	s_sleep 10
	s_cbranch_scc1 .LBB0_1396
	global_load_dword v2, v1, s[12:13] sc1
	s_waitcnt vmcnt(0)
	v_cmp_eq_u32_e32 vcc, 0, v2
	s_cbranch_vccnz .LBB0_1398
	s_mov_b64 s[22:23], 0
	s_mov_b64 s[20:21], -1

.LBB0_1491:
	global_load_dword v16, v17, s[8:9] sc1
	global_load_dword v1, v17, s[10:11] sc1
	global_load_dword v2, v17, s[12:13] sc1
	global_load_dword v3, v17, s[14:15] sc1
	global_load_dword v4, v17, s[16:17] sc1
	global_load_dword v5, v17, s[18:19] sc1
	global_load_dword v6, v17, s[22:23] sc1
	global_load_dword v7, v17, s[24:25] sc1
	global_load_dword v8, v17, s[26:27] sc1
	global_load_dword v9, v17, s[28:29] sc1
	global_load_dword v10, v17, s[30:31] sc1
	global_load_dword v11, v17, s[34:35] sc1
	global_load_dword v12, v17, s[36:37] sc1
	global_load_dword v13, v17, s[38:39] sc1
	global_load_dword v14, v17, s[40:41] sc1
	global_load_dword v15, v17, s[42:43] sc1
	s_mov_b64 s[44:45], -1
	s_mov_b64 s[46:47], -1
	s_waitcnt vmcnt(14)
	v_add_u32_e32 v18, v1, v16
	s_waitcnt vmcnt(13)
	v_add_u32_e32 v18, v18, v2
	s_waitcnt vmcnt(12)
	v_add_u32_e32 v18, v18, v3
	s_waitcnt vmcnt(11)
	v_add_u32_e32 v18, v18, v4
	s_waitcnt vmcnt(10)
	v_add_u32_e32 v18, v18, v5
	s_waitcnt vmcnt(9)
	v_add_u32_e32 v18, v18, v6
	s_waitcnt vmcnt(8)
	v_add_u32_e32 v18, v18, v7
	s_waitcnt vmcnt(7)
	v_add_u32_e32 v18, v18, v8
	s_waitcnt vmcnt(6)
	v_add_u32_e32 v18, v18, v9
	s_waitcnt vmcnt(5)
	v_add_u32_e32 v18, v18, v10
	s_waitcnt vmcnt(4)
	v_add_u32_e32 v18, v18, v11
	s_waitcnt vmcnt(3)
	v_add_u32_e32 v18, v18, v12
	s_waitcnt vmcnt(2)
	v_add_u32_e32 v18, v18, v13
	s_waitcnt vmcnt(1)
	v_add_u32_e32 v18, v18, v14
	s_waitcnt vmcnt(0)
	v_add_u32_e32 v18, v18, v15
	v_cmp_eq_u32_e32 vcc, s33, v18
	s_cbranch_vccnz .LBB0_1490
	s_and_b32 s44, s50, 0xff
	s_cmp_eq_u32 s44, 0
	s_mov_b64 s[44:45], -1
	s_mov_b64 s[48:49], -1
	s_sleep 10
	s_cbranch_scc0 .LBB0_1495
	global_load_dword v18, v17, s[6:7] sc1
	s_waitcnt vmcnt(0)
	v_cmp_eq_u32_e32 vcc, 0, v18
	s_cbranch_vccnz .LBB0_1497
	s_mov_b64 s[48:49], 0

.LBB0_1509:
	s_and_b32 s24, s28, 0xff
	s_mov_b64 s[22:23], -1
	s_cmp_lg_u32 s24, 0
	s_mov_b64 s[26:27], -1
	s_sleep 10
	s_cbranch_scc1 .LBB0_1512
	global_load_dword v3, v1, s[12:13] sc1
	s_waitcnt vmcnt(0)
	v_cmp_eq_u32_e32 vcc, 0, v3
	s_cbranch_vccnz .LBB0_1514
	s_mov_b64 s[26:27], 0
	s_mov_b64 s[24:25], -1

.LBB0_1526:
	s_and_b32 s22, s28, 0xff
	s_cmp_lg_u32 s22, 0
	s_mov_b64 s[24:25], -1
	s_sleep 10
	s_cbranch_scc1 .LBB0_1529
	global_load_dword v2, v1, s[12:13] sc1
	s_waitcnt vmcnt(0)
	v_cmp_eq_u32_e32 vcc, 0, v2
	s_cbranch_vccnz .LBB0_1531
	s_mov_b64 s[24:25], 0
	s_mov_b64 s[22:23], -1

.LBB0_2204:
	global_load_dword v16, v17, s[6:7] sc1
	global_load_dword v1, v17, s[8:9] sc1
	global_load_dword v2, v17, s[10:11] sc1
	global_load_dword v3, v17, s[12:13] sc1
	global_load_dword v4, v17, s[14:15] sc1
	global_load_dword v5, v17, s[16:17] sc1
	global_load_dword v6, v17, s[18:19] sc1
	global_load_dword v7, v17, s[22:23] sc1
	global_load_dword v8, v17, s[24:25] sc1
	global_load_dword v9, v17, s[26:27] sc1
	global_load_dword v10, v17, s[28:29] sc1
	global_load_dword v11, v17, s[30:31] sc1
	global_load_dword v12, v17, s[34:35] sc1
	global_load_dword v13, v17, s[36:37] sc1
	global_load_dword v14, v17, s[38:39] sc1
	global_load_dword v15, v17, s[40:41] sc1
	s_mov_b64 s[42:43], -1
	s_mov_b64 s[44:45], -1
	s_waitcnt vmcnt(14)
	v_add_u32_e32 v18, v1, v16
	s_waitcnt vmcnt(13)
	v_add_u32_e32 v18, v18, v2
	s_waitcnt vmcnt(12)
	v_add_u32_e32 v18, v18, v3
	s_waitcnt vmcnt(11)
	v_add_u32_e32 v18, v18, v4
	s_waitcnt vmcnt(10)
	v_add_u32_e32 v18, v18, v5
	s_waitcnt vmcnt(9)
	v_add_u32_e32 v18, v18, v6
	s_waitcnt vmcnt(8)
	v_add_u32_e32 v18, v18, v7
	s_waitcnt vmcnt(7)
	v_add_u32_e32 v18, v18, v8
	s_waitcnt vmcnt(6)
	v_add_u32_e32 v18, v18, v9
	s_waitcnt vmcnt(5)
	v_add_u32_e32 v18, v18, v10
	s_waitcnt vmcnt(4)
	v_add_u32_e32 v18, v18, v11
	s_waitcnt vmcnt(3)
	v_add_u32_e32 v18, v18, v12
	s_waitcnt vmcnt(2)
	v_add_u32_e32 v18, v18, v13
	s_waitcnt vmcnt(1)
	v_add_u32_e32 v18, v18, v14
	s_waitcnt vmcnt(0)
	v_add_u32_e32 v18, v18, v15
	v_cmp_eq_u32_e32 vcc, s33, v18
	s_cbranch_vccnz .LBB0_2203
	s_and_b32 s42, s48, 0xff
	s_cmp_eq_u32 s42, 0
	s_mov_b64 s[42:43], -1
	s_mov_b64 s[46:47], -1
	s_sleep 10
	s_cbranch_scc0 .LBB0_2208
	global_load_dword v18, v17, s[4:5] sc1
	s_waitcnt vmcnt(0)
	v_cmp_eq_u32_e32 vcc, 0, v18
	s_cbranch_vccnz .LBB0_2210
	s_mov_b64 s[46:47], 0

.LBB0_2222:
	s_and_b32 s22, s26, 0xff
	s_mov_b64 s[18:19], -1
	s_cmp_lg_u32 s22, 0
	s_mov_b64 s[24:25], -1
	s_sleep 10
	s_cbranch_scc1 .LBB0_2225
	global_load_dword v3, v1, s[10:11] sc1
	s_waitcnt vmcnt(0)
	v_cmp_eq_u32_e32 vcc, 0, v3
	s_cbranch_vccnz .LBB0_2227
	s_mov_b64 s[24:25], 0
	s_mov_b64 s[22:23], -1

.LBB0_2239:
	s_and_b32 s18, s26, 0xff
	s_cmp_lg_u32 s18, 0
	s_mov_b64 s[22:23], -1
	s_sleep 10
	s_cbranch_scc1 .LBB0_2242
	global_load_dword v2, v1, s[10:11] sc1
	s_waitcnt vmcnt(0)
	v_cmp_eq_u32_e32 vcc, 0, v2
	s_cbranch_vccnz .LBB0_2244
	s_mov_b64 s[22:23], 0
	s_mov_b64 s[18:19], -1

.LBB0_2307:
	global_load_dword v16, v17, s[6:7] sc1
	global_load_dword v1, v17, s[8:9] sc1
	global_load_dword v2, v17, s[10:11] sc1
	global_load_dword v3, v17, s[12:13] sc1
	global_load_dword v4, v17, s[16:17] sc1
	global_load_dword v5, v17, s[18:19] sc1
	global_load_dword v6, v17, s[22:23] sc1
	global_load_dword v7, v17, s[24:25] sc1
	global_load_dword v8, v17, s[26:27] sc1
	global_load_dword v9, v17, s[28:29] sc1
	global_load_dword v10, v17, s[30:31] sc1
	global_load_dword v11, v17, s[34:35] sc1
	global_load_dword v12, v17, s[36:37] sc1
	global_load_dword v13, v17, s[38:39] sc1
	global_load_dword v14, v17, s[40:41] sc1
	global_load_dword v15, v17, s[42:43] sc1
	s_mov_b64 s[44:45], -1
	s_mov_b64 s[46:47], -1
	s_waitcnt vmcnt(14)
	v_add_u32_e32 v18, v1, v16
	s_waitcnt vmcnt(13)
	v_add_u32_e32 v18, v18, v2
	s_waitcnt vmcnt(12)
	v_add_u32_e32 v18, v18, v3
	s_waitcnt vmcnt(11)
	v_add_u32_e32 v18, v18, v4
	s_waitcnt vmcnt(10)
	v_add_u32_e32 v18, v18, v5
	s_waitcnt vmcnt(9)
	v_add_u32_e32 v18, v18, v6
	s_waitcnt vmcnt(8)
	v_add_u32_e32 v18, v18, v7
	s_waitcnt vmcnt(7)
	v_add_u32_e32 v18, v18, v8
	s_waitcnt vmcnt(6)
	v_add_u32_e32 v18, v18, v9
	s_waitcnt vmcnt(5)
	v_add_u32_e32 v18, v18, v10
	s_waitcnt vmcnt(4)
	v_add_u32_e32 v18, v18, v11
	s_waitcnt vmcnt(3)
	v_add_u32_e32 v18, v18, v12
	s_waitcnt vmcnt(2)
	v_add_u32_e32 v18, v18, v13
	s_waitcnt vmcnt(1)
	v_add_u32_e32 v18, v18, v14
	s_waitcnt vmcnt(0)
	v_add_u32_e32 v18, v18, v15
	v_cmp_eq_u32_e32 vcc, s51, v18
	s_cbranch_vccnz .LBB0_2306
	s_and_b32 s44, s58, 0xff
	s_cmp_eq_u32 s44, 0
	s_mov_b64 s[44:45], -1
	s_mov_b64 s[48:49], -1
	s_sleep 10
	s_cbranch_scc0 .LBB0_2311
	global_load_dword v18, v17, s[4:5] sc1
	s_waitcnt vmcnt(0)
	v_cmp_eq_u32_e32 vcc, 0, v18
	s_cbranch_vccnz .LBB0_2313
	s_mov_b64 s[48:49], 0

.LBB0_2325:
	s_and_b32 s24, s28, 0xff
	s_mov_b64 s[22:23], -1
	s_cmp_lg_u32 s24, 0
	s_mov_b64 s[26:27], -1
	s_sleep 10
	s_cbranch_scc1 .LBB0_2328
	global_load_dword v3, v1, s[10:11] sc1
	s_waitcnt vmcnt(0)
	v_cmp_eq_u32_e32 vcc, 0, v3
	s_cbranch_vccnz .LBB0_2330
	s_mov_b64 s[26:27], 0
	s_mov_b64 s[24:25], -1

.LBB0_2342:
	s_and_b32 s22, s28, 0xff
	s_cmp_lg_u32 s22, 0
	s_mov_b64 s[24:25], -1
	s_sleep 10
	s_cbranch_scc1 .LBB0_2345
	global_load_dword v2, v1, s[10:11] sc1
	s_waitcnt vmcnt(0)
	v_cmp_eq_u32_e32 vcc, 0, v2
	s_cbranch_vccnz .LBB0_2347
	s_mov_b64 s[24:25], 0
	s_mov_b64 s[22:23], -1

.LBB0_2378:
	global_load_dword v16, v17, s[8:9] sc1
	global_load_dword v1, v17, s[10:11] sc1
	global_load_dword v2, v17, s[12:13] sc1
	global_load_dword v3, v17, s[16:17] sc1
	global_load_dword v4, v17, s[18:19] sc1
	global_load_dword v5, v17, s[22:23] sc1
	global_load_dword v6, v17, s[24:25] sc1
	global_load_dword v7, v17, s[26:27] sc1
	global_load_dword v8, v17, s[28:29] sc1
	global_load_dword v9, v17, s[30:31] sc1
	global_load_dword v10, v17, s[34:35] sc1
	global_load_dword v11, v17, s[36:37] sc1
	global_load_dword v12, v17, s[38:39] sc1
	global_load_dword v13, v17, s[40:41] sc1
	global_load_dword v14, v17, s[42:43] sc1
	global_load_dword v15, v17, s[44:45] sc1
	s_mov_b64 s[46:47], -1
	s_mov_b64 s[48:49], -1
	s_waitcnt vmcnt(14)
	v_add_u32_e32 v18, v1, v16
	s_waitcnt vmcnt(13)
	v_add_u32_e32 v18, v18, v2
	s_waitcnt vmcnt(12)
	v_add_u32_e32 v18, v18, v3
	s_waitcnt vmcnt(11)
	v_add_u32_e32 v18, v18, v4
	s_waitcnt vmcnt(10)
	v_add_u32_e32 v18, v18, v5
	s_waitcnt vmcnt(9)
	v_add_u32_e32 v18, v18, v6
	s_waitcnt vmcnt(8)
	v_add_u32_e32 v18, v18, v7
	s_waitcnt vmcnt(7)
	v_add_u32_e32 v18, v18, v8
	s_waitcnt vmcnt(6)
	v_add_u32_e32 v18, v18, v9
	s_waitcnt vmcnt(5)
	v_add_u32_e32 v18, v18, v10
	s_waitcnt vmcnt(4)
	v_add_u32_e32 v18, v18, v11
	s_waitcnt vmcnt(3)
	v_add_u32_e32 v18, v18, v12
	s_waitcnt vmcnt(2)
	v_add_u32_e32 v18, v18, v13
	s_waitcnt vmcnt(1)
	v_add_u32_e32 v18, v18, v14
	s_waitcnt vmcnt(0)
	v_add_u32_e32 v18, v18, v15
	v_cmp_eq_u32_e32 vcc, s59, v18
	s_cbranch_vccnz .LBB0_2377
	s_and_b32 s46, s60, 0xff
	s_cmp_eq_u32 s46, 0
	s_mov_b64 s[46:47], -1
	s_mov_b64 s[50:51], -1
	s_sleep 10
	s_cbranch_scc0 .LBB0_2382
	global_load_dword v18, v17, s[6:7] sc1
	s_waitcnt vmcnt(0)
	v_cmp_eq_u32_e32 vcc, 0, v18
	s_cbranch_vccnz .LBB0_2384
	s_mov_b64 s[50:51], 0

.LBB0_2396:
	s_and_b32 s26, s30, 0xff
	s_mov_b64 s[24:25], -1
	s_cmp_lg_u32 s26, 0
	s_mov_b64 s[28:29], -1
	s_sleep 10
	s_cbranch_scc1 .LBB0_2399
	global_load_dword v3, v1, s[12:13] sc1
	s_waitcnt vmcnt(0)
	v_cmp_eq_u32_e32 vcc, 0, v3
	s_cbranch_vccnz .LBB0_2401
	s_mov_b64 s[28:29], 0
	s_mov_b64 s[26:27], -1

.LBB0_2413:
	s_and_b32 s24, s30, 0xff
	s_cmp_lg_u32 s24, 0
	s_mov_b64 s[26:27], -1
	s_sleep 10
	s_cbranch_scc1 .LBB0_2416
	global_load_dword v2, v1, s[12:13] sc1
	s_waitcnt vmcnt(0)
	v_cmp_eq_u32_e32 vcc, 0, v2
	s_cbranch_vccnz .LBB0_2418
	s_mov_b64 s[26:27], 0
	s_mov_b64 s[24:25], -1

.LBB0_2453:
	global_load_dword v15, v16, s[6:7] sc1
	global_load_dword v0, v16, s[8:9] sc1
	global_load_dword v1, v16, s[10:11] sc1
	global_load_dword v2, v16, s[12:13] sc1
	global_load_dword v3, v16, s[16:17] sc1
	global_load_dword v4, v16, s[18:19] sc1
	global_load_dword v5, v16, s[22:23] sc1
	global_load_dword v6, v16, s[24:25] sc1
	global_load_dword v7, v16, s[26:27] sc1
	global_load_dword v8, v16, s[28:29] sc1
	global_load_dword v9, v16, s[30:31] sc1
	global_load_dword v10, v16, s[34:35] sc1
	global_load_dword v11, v16, s[36:37] sc1
	global_load_dword v12, v16, s[38:39] sc1
	global_load_dword v13, v16, s[40:41] sc1
	global_load_dword v14, v16, s[42:43] sc1
	s_mov_b64 s[44:45], -1
	s_mov_b64 s[46:47], -1
	s_waitcnt vmcnt(14)
	v_add_u32_e32 v17, v0, v15
	s_waitcnt vmcnt(13)
	v_add_u32_e32 v17, v17, v1
	s_waitcnt vmcnt(12)
	v_add_u32_e32 v17, v17, v2
	s_waitcnt vmcnt(11)
	v_add_u32_e32 v17, v17, v3
	s_waitcnt vmcnt(10)
	v_add_u32_e32 v17, v17, v4
	s_waitcnt vmcnt(9)
	v_add_u32_e32 v17, v17, v5
	s_waitcnt vmcnt(8)
	v_add_u32_e32 v17, v17, v6
	s_waitcnt vmcnt(7)
	v_add_u32_e32 v17, v17, v7
	s_waitcnt vmcnt(6)
	v_add_u32_e32 v17, v17, v8
	s_waitcnt vmcnt(5)
	v_add_u32_e32 v17, v17, v9
	s_waitcnt vmcnt(4)
	v_add_u32_e32 v17, v17, v10
	s_waitcnt vmcnt(3)
	v_add_u32_e32 v17, v17, v11
	s_waitcnt vmcnt(2)
	v_add_u32_e32 v17, v17, v12
	s_waitcnt vmcnt(1)
	v_add_u32_e32 v17, v17, v13
	s_waitcnt vmcnt(0)
	v_add_u32_e32 v17, v17, v14
	v_cmp_eq_u32_e32 vcc, s33, v17
	s_cbranch_vccnz .LBB0_2452
	s_and_b32 s44, s50, 0xff
	s_cmp_eq_u32 s44, 0
	s_mov_b64 s[44:45], -1
	s_mov_b64 s[48:49], -1
	s_sleep 10
	s_cbranch_scc0 .LBB0_2457
	global_load_dword v17, v16, s[4:5] sc1
	s_waitcnt vmcnt(0)
	v_cmp_eq_u32_e32 vcc, 0, v17
	s_cbranch_vccnz .LBB0_2459
	s_mov_b64 s[48:49], 0

.LBB0_2471:
	s_and_b32 s24, s28, 0xff
	s_mov_b64 s[22:23], -1
	s_cmp_lg_u32 s24, 0
	s_mov_b64 s[26:27], -1
	s_sleep 10
	s_cbranch_scc1 .LBB0_2474
	global_load_dword v2, v0, s[10:11] sc1
	s_waitcnt vmcnt(0)
	v_cmp_eq_u32_e32 vcc, 0, v2
	s_cbranch_vccnz .LBB0_2476
	s_mov_b64 s[26:27], 0
	s_mov_b64 s[24:25], -1

.LBB0_2488:
	s_and_b32 s22, s28, 0xff
	s_cmp_lg_u32 s22, 0
	s_mov_b64 s[24:25], -1
	s_sleep 10
	s_cbranch_scc1 .LBB0_2491
	global_load_dword v1, v0, s[10:11] sc1
	s_waitcnt vmcnt(0)
	v_cmp_eq_u32_e32 vcc, 0, v1
	s_cbranch_vccnz .LBB0_2493
	s_mov_b64 s[24:25], 0
	s_mov_b64 s[22:23], -1
